# P20: small 4-group start stagger of all workgroups ((bid&3) x 1 sleep step) to spread the residual-epilogue HBM bursts
# speedup vs baseline: 1.0038x; 1.0038x over previous
.LBB0_2578:
.LBB0_2579:
	s_and_b32 s98, s26, 3
	s_mul_i32 s98, s98, 1
	s_cmp_eq_u32 s98, 0
	s_cbranch_scc1 .Lstag20_done
.Lstag20_loop:
	s_sleep 127
	s_add_i32 s98, s98, -1
	s_cmp_lg_u32 s98, 0
	s_cbranch_scc1 .Lstag20_loop
.Lstag20_done:
	s_cmp_gt_i32 s40, 20
	s_cselect_b64 s[2:3], -1, 0
	s_cmp_lt_i32 s41, 21
	s_cselect_b64 s[4:5], -1, 0
	s_or_b64 s[2:3], s[2:3], s[4:5]
	s_and_b64 vcc, exec, s[2:3]
	s_cbranch_vccnz .LBB0_2722
	v_mov_b32_e32 v2, v0
	s_cmpk_lt_i32 s26, 0x400
	s_waitcnt lgkmcnt(0)
	s_movk_i32 s12, 0x600
	v_readfirstlane_b32 s14, v2
	s_movk_i32 s16, 0x600
	s_movk_i32 s10, 0x600
	s_cselect_b64 s[2:3], -1, 0
	s_cmpk_gt_i32 s26, 0x3ff
	s_cbranch_scc1 .LBB0_2583
	s_ashr_i32 s4, s26, 31
	s_lshr_b32 s4, s4, 29
	s_add_i32 s6, s26, s4
	s_and_b32 s4, s6, -8
	s_sub_i32 s7, s26, s4
	s_cmp_gt_i32 s7, -1
	s_cbranch_scc0 .LBB0_2668
	s_lshl_b32 s8, s7, 7
	s_cbranch_execz .LBB0_2669
	s_branch .LBB0_2670
